# stacked + input-projection K-loop LDS-DMA loads use SGPR-base + 32-bit lane offset addressing (18 per-load 64-bit VALU address adds removed)
# baseline (speedup 1.0000x reference)
.LBB0_185:
	s_ashr_i32 s23, s22, 31
	s_lshl_b64 s[24:25], s[22:23], 19
	s_add_u32 s24, s19, s24
	s_addc_u32 s25, s33, s25
	s_and_b64 s[26:27], s[4:5], exec
	s_cselect_b32 s7, s25, s35
	s_cselect_b32 s9, s24, s34
	s_ashr_i32 s21, s20, 31
	s_lshl_b64 s[26:27], s[20:21], 19
	s_add_u32 s26, s38, s26
	s_addc_u32 s27, s39, s27
	s_and_b64 s[36:37], s[4:5], exec
	s_cselect_b32 s21, s27, s31
	s_cselect_b32 s23, s26, s30
	s_add_u32 s53, s30, 0x4000
	s_addc_u32 s54, s31, 0
	s_add_u32 s30, s34, 0x40080
	s_addc_u32 s31, s35, 0
	s_mov_b32 s55, -2
	ds_read_b128 v[26:29], v191
	ds_read_b128 v[30:33], v191 offset:1024
	ds_read_b128 v[18:21], v191 offset:2048
	ds_read_b128 v[22:25], v191 offset:3072
	ds_read_b128 v[10:13], v192
	ds_read_b128 v[14:17], v192 offset:1024
	ds_read_b128 v[2:5], v192 offset:2048
	ds_read_b128 v[6:9], v192 offset:3072
	s_add_u32 s0, s30, 0xfffc0080
	s_addc_u32 s1, s31, -1
	s_cmp_eq_u32 s55, 12
	s_cselect_b32 s37, s7, s1
	s_cselect_b32 s36, s9, s0
	s_cselect_b32 s35, s21, s54
	s_cselect_b32 s34, s23, s53
	s_add_i32 m0, s29, 0xc000
	ds_read_b128 v[196:199], v193
	ds_read_b128 v[200:203], v193 offset:1024
	ds_read_b128 v[204:207], v193 offset:2048
	ds_read_b128 v[208:211], v193 offset:3072
	ds_read_b128 v[212:215], v193 offset:4096
	ds_read_b128 v[216:219], v193 offset:5120
	ds_read_b128 v[220:223], v193 offset:6144
	ds_read_b128 v[224:227], v193 offset:7168
	global_load_lds_dwordx4 v176, s[30:31]
	s_add_i32 m0, s29, 0xe000
	s_nop 0
	global_load_lds_dwordx4 v178, s[30:31]
	s_and_b64 vcc, exec, s[14:15]
	s_cbranch_vccnz .Lwa_186p_0
	s_waitcnt vmcnt(8)

.Lwb_186p_0:
	s_setprio 0
	s_barrier
	s_add_i32 s0, s49, s40
	s_mov_b32 m0, s0
	ds_read_b128 v[196:199], v193 offset:16384
	ds_read_b128 v[200:203], v193 offset:17408
	ds_read_b128 v[204:207], v193 offset:18432
	ds_read_b128 v[208:211], v193 offset:19456
	ds_read_b128 v[212:215], v193 offset:20480
	ds_read_b128 v[216:219], v193 offset:21504
	ds_read_b128 v[220:223], v193 offset:22528
	ds_read_b128 v[224:227], v193 offset:23552
	global_load_lds_dwordx4 v164, s[34:35]
	s_add_i32 m0, s0, 0x2000
	s_add_u32 s56, s34, 0x40000
	s_addc_u32 s57, s35, 0
	s_add_i32 s0, s50, s40
	global_load_lds_dwordx4 v168, s[34:35]
	s_mov_b32 m0, s0
	v_lshl_add_u64 v[186:187], s[36:37], 0, v[166:167]
	global_load_lds_dwordx4 v164, s[56:57]
	s_add_i32 m0, s0, 0x2000
	s_nop 0
	global_load_lds_dwordx4 v168, s[56:57]
	v_lshl_add_u64 v[184:185], s[36:37], 0, v[162:163]
	s_mov_b32 m0, s29
	s_nop 0
	global_load_lds_dwordx4 v[184:185], off
	s_mov_b32 m0, s41
	s_nop 0
	global_load_lds_dwordx4 v[186:187], off
	s_and_b64 vcc, exec, s[14:15]
	s_cbranch_vccnz .Lwa_186p_1
	s_waitcnt vmcnt(8)

.LBB0_186:
	ds_read_b128 v[26:29], v191
	ds_read_b128 v[30:33], v191 offset:1024
	ds_read_b128 v[18:21], v191 offset:2048
	ds_read_b128 v[22:25], v191 offset:3072
	ds_read_b128 v[10:13], v192
	ds_read_b128 v[14:17], v192 offset:1024
	ds_read_b128 v[2:5], v192 offset:2048
	ds_read_b128 v[6:9], v192 offset:3072
	s_add_u32 s0, s30, 0xfffc0080
	s_addc_u32 s1, s31, -1
	s_cmp_eq_u32 s55, 12
	s_cselect_b32 s37, s7, s1
	s_cselect_b32 s36, s9, s0
	s_cselect_b32 s35, s21, s54
	s_cselect_b32 s34, s23, s53
	s_add_i32 m0, s29, 0xc000
	ds_read_b128 v[196:199], v193
	ds_read_b128 v[200:203], v193 offset:1024
	ds_read_b128 v[204:207], v193 offset:2048
	ds_read_b128 v[208:211], v193 offset:3072
	ds_read_b128 v[212:215], v193 offset:4096
	ds_read_b128 v[216:219], v193 offset:5120
	ds_read_b128 v[220:223], v193 offset:6144
	ds_read_b128 v[224:227], v193 offset:7168
	global_load_lds_dwordx4 v176, s[30:31]
	s_add_i32 m0, s29, 0xe000
	s_nop 0
	global_load_lds_dwordx4 v178, s[30:31]
	s_and_b64 vcc, exec, s[14:15]
	s_cbranch_vccnz .Lwa_186l_0
	s_waitcnt vmcnt(8)

.Lmid_186:
	s_add_i32 s0, 0, 0x18000
	v_add_u32_e32 v0, s0, v189
	s_add_i32 s1, 0, 0x1c000
	ds_read_b128 v[2:5], v0
	ds_read_b128 v[6:9], v0 offset:1024
	ds_read_b128 v[10:13], v0 offset:2048
	ds_read_b128 v[14:17], v0 offset:3072
	v_add_u32_e32 v0, s1, v189
	ds_read_b128 v[18:21], v0
	ds_read_b128 v[22:25], v0 offset:1024
	ds_read_b128 v[26:29], v0 offset:2048
	ds_read_b128 v[30:33], v0 offset:3072
	s_add_u32 s36, s36, 0x40000
	s_addc_u32 s37, s37, 0
	s_mov_b32 m0, s42
	ds_read_b128 v[196:199], v193 offset:32768
	ds_read_b128 v[200:203], v193 offset:33792
	ds_read_b128 v[204:207], v193 offset:34816
	ds_read_b128 v[208:211], v193 offset:35840
	ds_read_b128 v[212:215], v193 offset:36864
	ds_read_b128 v[216:219], v193 offset:37888
	ds_read_b128 v[220:223], v193 offset:38912
	ds_read_b128 v[224:227], v193 offset:39936
	global_load_lds_dwordx4 v162, s[36:37]
	s_mov_b32 m0, s43
	s_nop 0
	global_load_lds_dwordx4 v166, s[36:37]
	s_and_b64 vcc, exec, s[14:15]
	s_cbranch_vccnz .Lwa_186l_2
	s_waitcnt vmcnt(8)

.Lwb_186l_2:
	s_setprio 0
	s_barrier
	s_add_u32 s36, s34, 0x2000
	s_addc_u32 s37, s35, 0
	s_add_i32 s0, s0, s40
	s_mov_b32 m0, s0
	ds_read_b128 v[196:199], v193 offset:49152
	ds_read_b128 v[200:203], v193 offset:50176
	ds_read_b128 v[204:207], v193 offset:51200
	ds_read_b128 v[208:211], v193 offset:52224
	ds_read_b128 v[212:215], v193 offset:53248
	ds_read_b128 v[216:219], v193 offset:54272
	ds_read_b128 v[220:223], v193 offset:55296
	ds_read_b128 v[224:227], v193 offset:56320
	global_load_lds_dwordx4 v164, s[36:37]
	s_add_i32 m0, s0, 0x2000
	s_add_u32 s34, s34, 0x42000
	s_addc_u32 s35, s35, 0
	s_add_i32 s0, s1, s40
	global_load_lds_dwordx4 v168, s[36:37]
	s_mov_b32 m0, s0
	v_lshl_add_u64 v[184:185], v[184:185], 0, s[12:13]
	global_load_lds_dwordx4 v164, s[34:35]
	s_add_i32 m0, s0, 0x2000
	s_nop 0
	global_load_lds_dwordx4 v168, s[34:35]
	s_mov_b32 m0, s44
	s_nop 0
	global_load_lds_dwordx4 v[184:185], off
	v_lshl_add_u64 v[184:185], v[186:187], 0, s[12:13]
	s_mov_b32 m0, s45
	s_nop 0
	global_load_lds_dwordx4 v[184:185], off
	s_and_b64 vcc, exec, s[14:15]
	s_cbranch_vccnz .Lwa_186l_3
	s_waitcnt vmcnt(8)
